# M1 unit-loop top: two serial LDS round trips whose results were never used (volatile reads of cnt[e]/pre[e] for an unused nv) removed; on top of m23
# baseline (speedup 1.0000x reference)
; DI int rfl(int v) { return __builtin_amdgcn_readfirstlane(v); }
;     DI bool next(int i, Unit& u) const {
;         const int L = i * G + c; if (L >= ntot) return false;
;         const int rt = L / NC; u.pn = L - rt * NC; u.pm = rt;
;         int e = 0;
; #pragma unroll
;         for (int j = 1; j < 16; ++j) e += (rt >= rfl(pre[j])) ? 1 : 0;
;         e = rfl(e); u.e = e; const int rem = rfl(cnt[e]) - 256 * (rt - rfl(pre[e])); u.nv = rem < 256 ? rem : 256; u.ui = i; return true;
; template <class Epi, class Sched, bool F8 = false>
; DI void gemm_phase(LAS unsigned char* lds, const int K, const Sched& S, const Epi& E) {
;     ...
;         const bool has_next = S.next(ui + 1, nxt);
.LBB0_1357:
	s_add_i32 s89, s89, 1
	s_mul_i32 s6, s89, s39
	s_add_i32 s6, s6, s78
	s_cmp_lt_i32 s6, s79
	s_cselect_b64 s[74:75], -1, 0
	s_cmp_ge_i32 s6, s79
	s_cbranch_scc1 .LBB0_1359
	s_ashr_i32 s7, s6, 31
	s_lshr_b32 s7, s7, 29
	v_lshl_add_u32 v6, v202, 2, s76
	ds_read_b32 v6, v6
	s_add_i32 s7, s6, s7
	s_ashr_i32 s92, s7, 3
	s_and_b32 s7, s7, -8
	s_sub_i32 s66, s6, s7
	s_mov_b32 s91, s89
	s_waitcnt lgkmcnt(0)
	v_cmp_le_i32_e64 s[6:7], v6, s92
	s_and_b32 s6, s6, 0xfffe
	s_bcnt1_i32_b32 s56, s6
	s_lshl_b32 s6, s56, 2
	s_add_i32 s7, s13, s6
	s_add_i32 s6, s76, s6
